# norm1 row loop: dropped the top-of-iteration full memory wait that only waited for the previous row's output stores (on top of v102)
# speedup vs baseline: 1.0112x; 1.0112x over previous
.LBB0_350:
	s_add_u32 s0, s16, 1
	s_addc_u32 s1, s17, 0
	s_cmp_ge_i32 s0, s28
	s_cselect_b64 s[18:19], -1, 0
	v_mov_b64_e32 v[78:79], v[6:7]
	v_mov_b64_e32 v[74:75], v[22:23]
	v_mov_b64_e32 v[70:71], v[26:27]
	v_mov_b64_e32 v[66:67], v[30:31]
	s_and_b64 vcc, exec, s[18:19]
	v_mov_b64_e32 v[76:77], v[4:5]
	v_mov_b64_e32 v[72:73], v[20:21]
	v_mov_b64_e32 v[68:69], v[24:25]
	v_mov_b64_e32 v[64:65], v[28:29]
	s_cbranch_vccnz .LBB0_353
	v_lshl_add_u64 v[64:65], s[10:11], 0, v[112:113]
	v_add_co_u32_e32 v76, vcc, 0x1000, v64
	s_nop 1
	v_addc_co_u32_e32 v77, vcc, 0, v65, vcc
	global_load_dwordx4 v[64:67], v[76:77], off
	global_load_dwordx4 v[68:71], v[76:77], off offset:1024
	global_load_dwordx4 v[72:75], v[76:77], off offset:2048
	s_nop 0
	global_load_dwordx4 v[76:79], v[76:77], off offset:3072
	s_andn2_b64 vcc, exec, s[8:9]
	s_mov_b64 s[20:21], -1
	s_cbranch_vccz .LBB0_354
